# idle half of the grid in the F2 phase pre-reads the two gate byte arrays; merge-GEMM epilogue issues its 32 gate loads together (one wait)
# speedup vs baseline: 1.0074x; 1.0074x over previous
.LBB0_1606:
	s_cmpk_lt_u32 s6, 0x80
	s_cbranch_scc1 .LBB0_1612
	s_lshl_b32 s2, s6, 3
	v_readlane_b32 s0, v255, 7
	s_add_i32 s2, s2, s0
	s_add_i32 s5, s2, 0xfffffc00
	s_lshl_b32 s0, s5, 14
	v_lshlrev_b32_e32 v204, 4, v254
	v_add_u32_e32 v204, s0, v204
	v_mov_b32_e32 v205, v204
	s_add_u32 s0, s50, 0x6800000
	s_addc_u32 s1, s51, 0
	global_load_dwordx4 v[200:203], v204, s[0:1]
	global_load_dwordx4 v[200:203], v204, s[0:1] offset:1024
	global_load_dwordx4 v[200:203], v204, s[0:1] offset:2048
	global_load_dwordx4 v[200:203], v204, s[0:1] offset:3072
	v_add_u32_e32 v204, 0x1000, v204
	global_load_dwordx4 v[200:203], v204, s[0:1]
	global_load_dwordx4 v[200:203], v204, s[0:1] offset:1024
	global_load_dwordx4 v[200:203], v204, s[0:1] offset:2048
	global_load_dwordx4 v[200:203], v204, s[0:1] offset:3072
	v_add_u32_e32 v204, 0x1000, v204
	global_load_dwordx4 v[200:203], v204, s[0:1]
	global_load_dwordx4 v[200:203], v204, s[0:1] offset:1024
	global_load_dwordx4 v[200:203], v204, s[0:1] offset:2048
	global_load_dwordx4 v[200:203], v204, s[0:1] offset:3072
	v_add_u32_e32 v204, 0x1000, v204
	global_load_dwordx4 v[200:203], v204, s[0:1]
	global_load_dwordx4 v[200:203], v204, s[0:1] offset:1024
	global_load_dwordx4 v[200:203], v204, s[0:1] offset:2048
	global_load_dwordx4 v[200:203], v204, s[0:1] offset:3072
	s_add_u32 s0, s50, 0x8800000
	s_addc_u32 s1, s51, 0
	global_load_dwordx4 v[200:203], v205, s[0:1]
	global_load_dwordx4 v[200:203], v205, s[0:1] offset:1024
	global_load_dwordx4 v[200:203], v205, s[0:1] offset:2048
	global_load_dwordx4 v[200:203], v205, s[0:1] offset:3072
	v_add_u32_e32 v205, 0x1000, v205
	global_load_dwordx4 v[200:203], v205, s[0:1]
	global_load_dwordx4 v[200:203], v205, s[0:1] offset:1024
	global_load_dwordx4 v[200:203], v205, s[0:1] offset:2048
	global_load_dwordx4 v[200:203], v205, s[0:1] offset:3072
	v_add_u32_e32 v205, 0x1000, v205
	global_load_dwordx4 v[200:203], v205, s[0:1]
	global_load_dwordx4 v[200:203], v205, s[0:1] offset:1024
	global_load_dwordx4 v[200:203], v205, s[0:1] offset:2048
	global_load_dwordx4 v[200:203], v205, s[0:1] offset:3072
	v_add_u32_e32 v205, 0x1000, v205
	global_load_dwordx4 v[200:203], v205, s[0:1]
	global_load_dwordx4 v[200:203], v205, s[0:1] offset:1024
	global_load_dwordx4 v[200:203], v205, s[0:1] offset:2048
	global_load_dwordx4 v[200:203], v205, s[0:1] offset:3072
	s_and_b32 s0, s5, 0x380
	s_lshl_b32 s0, s0, 2
	v_or_b32_e32 v1, 64, v254
	s_add_u32 s0, s50, s0
	v_mul_lo_u32 v1, s5, v1
	s_waitcnt vmcnt(22)
	v_mul_lo_u32 v2, s5, v254
	s_addc_u32 s1, s51, 0
	v_and_b32_e32 v2, 0x7f, v2
	v_and_b32_e32 v1, 0x7f, v1
	s_add_u32 s3, s0, 0x182000
	v_cvt_f32_ubyte0_e32 v3, v2
	v_cvt_f32_ubyte0_e32 v2, v1
	s_mov_b32 s0, 0x3c800000
	s_addc_u32 s4, s1, 0
	s_waitcnt lgkmcnt(8)
	v_pk_mul_f32 v[4:5], v[2:3], s[0:1] op_sel_hi:[1,0]
	s_and_b32 s0, s5, 0x3ff
	s_add_u32 s0, s50, s0
	s_addc_u32 s1, s51, 0
	s_add_u32 s7, s0, 0x2a00000
	s_addc_u32 s8, s1, 0
	s_and_b32 s0, s5, 0xfffffc00
	s_ashr_i32 s1, s0, 31
	s_lshl_b64 s[0:1], s[0:1], 2
	s_add_u32 s0, s3, s0
	s_addc_u32 s1, s4, s1
	v_lshlrev_b32_e32 v2, 2, v254
	global_load_dword v1, v2, s[0:1]
	global_load_dword v8, v2, s[0:1] offset:256
	s_waitcnt vmcnt(23)
	v_pk_mul_f32 v[6:7], v[4:5], 0.5 op_sel_hi:[1,0]
	s_mov_b32 s0, 0x7f800000
	v_fract_f32_e32 v3, v7
	v_add_f32_e32 v3, v3, v3
	v_cmp_neq_f32_e32 vcc, s0, v7
	s_waitcnt vmcnt(22)
	v_mov_b32_e32 v11, 0xbf1f24be
	v_mov_b32_e32 v13, 0x40234736
	v_cndmask_b32_e32 v3, 0, v3, vcc
	v_cmp_lt_f32_e32 vcc, 1.0, v5
	s_waitcnt vmcnt(21)
	v_mov_b32_e32 v16, 0xbfaad1da
	s_waitcnt lgkmcnt(5)
	v_mov_b32_e32 v14, 0xc0a55e0e
	v_cndmask_b32_e32 v3, v5, v3, vcc
	v_add_f32_e32 v7, v3, v3
	v_rndne_f32_e32 v7, v7
	v_fmac_f32_e32 v3, -0.5, v7
	v_mul_f32_e32 v10, v3, v3
	v_fmamk_f32 v12, v10, 0x3e75aa41, v11
	v_fmaak_f32 v12, v10, v12, 0x40234736
	v_fmaak_f32 v12, v10, v12, 0xc0a55e0e
	s_waitcnt lgkmcnt(2)
	v_mul_f32_e32 v15, v3, v10
	v_cvt_i32_f32_e32 v9, v7
	v_mul_f32_e32 v12, v15, v12
	v_mov_b32_e32 v15, 0x3e642e9d
	v_fmac_f32_e32 v12, 0x40490fdb, v3
	v_fmamk_f32 v3, v10, 0x3d4be544, v15
	v_fmaak_f32 v3, v10, v3, 0xbfaad1da
	v_fmaak_f32 v3, v10, v3, 0x4081e0d3
	v_and_b32_e32 v7, 2, v9
	v_fmaak_f32 v3, v10, v3, 0xc09de9e6
	v_and_b32_e32 v9, 1, v9
	v_fma_f32 v3, v10, v3, 1.0
	v_cmp_eq_u32_e32 vcc, 0, v9
	v_fract_f32_e32 v9, v6
	v_add_f32_e32 v9, v9, v9
	v_cndmask_b32_e64 v3, -v12, v3, vcc
	v_cmp_eq_u32_e32 vcc, 0, v7
	v_mov_b32_e32 v17, 0x4081e0d3
	s_waitcnt vmcnt(20)
	v_mov_b32_e32 v18, 0xc09de9e6
	v_cndmask_b32_e64 v3, -v3, v3, vcc
	v_cmp_neq_f32_e32 vcc, s0, v6
	v_mov_b32_e32 v7, 0x7fc00000
	s_nop 0
	v_cndmask_b32_e32 v6, 0, v9, vcc
	v_cmp_lt_f32_e32 vcc, 1.0, v4
	s_nop 1
	v_cndmask_b32_e32 v6, v4, v6, vcc
	v_add_f32_e32 v9, v6, v6
	v_rndne_f32_e32 v9, v9
	v_fmac_f32_e32 v6, -0.5, v9
	v_cvt_i32_f32_e32 v10, v9
	v_mul_f32_e32 v9, v6, v6
	v_fmac_f32_e32 v11, 0x3e75aa41, v9
	v_fmac_f32_e32 v15, 0x3d4be544, v9
	v_fmac_f32_e32 v13, v9, v11
	v_fmac_f32_e32 v16, v9, v15
	v_fmac_f32_e32 v14, v9, v13
	v_mul_f32_e32 v11, v6, v9
	v_fmac_f32_e32 v17, v9, v16
	v_mul_f32_e32 v11, v11, v14
	v_fmac_f32_e32 v18, v9, v17
	v_cmp_lg_f32_e32 vcc, s0, v5
	v_fmac_f32_e32 v11, 0x40490fdb, v6
	v_fma_f32 v6, v9, v18, 1.0
	v_and_b32_e32 v9, 1, v10
	v_cndmask_b32_e32 v3, v7, v3, vcc
	v_and_b32_e32 v5, 2, v10
	v_cmp_eq_u32_e32 vcc, 0, v9
	s_nop 1
	v_cndmask_b32_e64 v6, -v11, v6, vcc
	v_cmp_eq_u32_e32 vcc, 0, v5
	s_nop 1
	v_cndmask_b32_e64 v5, -v6, v6, vcc
	v_cmp_lg_f32_e32 vcc, s0, v4
	s_nop 1
	v_cndmask_b32_e32 v4, v7, v5, vcc
	v_mbcnt_lo_u32_b32 v5, -1, 0
	v_mbcnt_hi_u32_b32 v10, -1, v5
	v_and_b32_e32 v5, 64, v10
	v_add_u32_e32 v11, 64, v5
	v_xor_b32_e32 v5, 1, v10
	v_cmp_lt_i32_e32 vcc, v5, v11
	s_waitcnt vmcnt(0)
	v_mul_f32_e32 v7, v4, v8
	v_fmac_f32_e32 v7, v3, v1
	v_cndmask_b32_e32 v5, v10, v5, vcc
	v_lshlrev_b32_e32 v5, 2, v5
	ds_bpermute_b32 v1, v5, v7
	v_xor_b32_e32 v6, 2, v10
	v_cmp_lt_i32_e32 vcc, v6, v11
	v_xor_b32_e32 v13, 32, v10
	s_waitcnt lgkmcnt(0)
	v_add_f32_e32 v1, v7, v1
	v_cndmask_b32_e32 v6, v10, v6, vcc
	v_lshlrev_b32_e32 v6, 2, v6
	ds_bpermute_b32 v8, v6, v1
	v_xor_b32_e32 v7, 4, v10
	v_cmp_lt_i32_e32 vcc, v7, v11
	s_waitcnt lgkmcnt(0)
	v_add_f32_e32 v1, v1, v8
	v_cndmask_b32_e32 v7, v10, v7, vcc
	v_lshlrev_b32_e32 v7, 2, v7
	ds_bpermute_b32 v9, v7, v1
	v_xor_b32_e32 v8, 8, v10
	v_cmp_lt_i32_e32 vcc, v8, v11
	s_waitcnt lgkmcnt(0)
	v_add_f32_e32 v1, v1, v9
	v_cndmask_b32_e32 v8, v10, v8, vcc
	v_lshlrev_b32_e32 v8, 2, v8
	ds_bpermute_b32 v12, v8, v1
	v_xor_b32_e32 v9, 16, v10
	v_cmp_lt_i32_e32 vcc, v9, v11
	s_waitcnt lgkmcnt(0)
	v_add_f32_e32 v1, v1, v12
	v_cndmask_b32_e32 v9, v10, v9, vcc
	v_lshlrev_b32_e32 v9, 2, v9
	ds_bpermute_b32 v12, v9, v1
	v_cmp_lt_i32_e32 vcc, v13, v11
	v_mov_b32_e32 v11, 0
	s_waitcnt lgkmcnt(0)
	v_add_f32_e32 v12, v1, v12
	v_cndmask_b32_e32 v10, v10, v13, vcc
	v_lshlrev_b32_e32 v10, 2, v10
	ds_bpermute_b32 v13, v10, v12
	v_cmp_eq_u32_e32 vcc, 0, v254
	s_and_saveexec_b64 s[0:1], vcc
	s_cbranch_execz .LBB0_1609
	s_waitcnt lgkmcnt(0)
	v_add_f32_e32 v1, v12, v13
	v_mul_f32_e32 v1, 0x3ab504f3, v1
	v_max_f32_e32 v1, 0xc3e00000, v1
	s_ashr_i32 s10, s5, 10
	v_min_f32_e32 v1, 0x43e00000, v1
	v_mov_b32_e32 v12, 0
	v_cvt_pk_fp8_f32 v12, v1, 0
	s_ashr_i32 s11, s10, 31
	s_lshl_b64 s[10:11], s[10:11], 23
	s_add_u32 s10, s7, s10
	s_addc_u32 s11, s8, s11
	global_store_byte v11, v12, s[10:11]
